# phase D prologue: the three prefix-state staging loads stay in flight together and are written to LDS after one wait (was three dependent round trips); phase I set-up LN1 parameter loads issued togeth
# speedup vs baseline: 1.0149x; 1.0027x over previous
.LBB0_614:
	s_or_b64 exec, exec, s[4:5]
	s_and_b64 s[4:5], s[8:9], exec
	s_mov_b32 s3, 0x65200000
	s_cselect_b32 s3, s3, 0x67200000
	s_add_u32 s4, s76, s3
	s_addc_u32 s5, s77, 0
	s_lshl_b32 s3, s21, 3
	s_lshl_b32 s6, s97, 1
	s_movk_i32 s7, 0x480
	s_or_b32 s3, s3, s6
	v_cmp_gt_i32_e32 vcc, s7, v80
	s_and_saveexec_b64 s[12:13], vcc
	s_cbranch_execz .LBB0_616
	s_mov_b32 s7, 0x38e38e39
	v_mul_hi_i32 v50, v80, s7
	v_lshrrev_b32_e32 v51, 31, v50
	v_ashrrev_i32_e32 v50, 7, v50
	v_add_u32_e32 v50, v50, v51
	v_mul_i32_i24_e32 v51, 0x240, v50
	v_sub_u32_e32 v51, v80, v51
	v_mul_i32_i24_e32 v52, 0x2aab, v51
	v_lshrrev_b32_e32 v53, 31, v52
	v_add_u16_sdwa v54, v52, v53 dst_sel:DWORD dst_unused:UNUSED_PAD src0_sel:WORD_1 src1_sel:DWORD
	v_mul_lo_u16_e32 v52, 6, v54
	v_add_u32_e32 v50, s3, v50
	v_sub_u16_e32 v55, v51, v52
	v_lshl_or_b32 v52, v50, 6, s18
	v_mov_b64_e32 v[50:51], s[4:5]
	s_movk_i32 s7, 0x2400
	v_mad_i64_i32 v[50:51], s[14:15], v52, s7, v[50:51]
	v_mul_i32_i24_sdwa v52, sext(v54), v199 dst_sel:DWORD dst_unused:UNUSED_PAD src0_sel:WORD_0 src1_sel:DWORD
	v_ashrrev_i32_e32 v53, 31, v52
	v_lshl_add_u64 v[50:51], v[52:53], 1, v[50:51]
	v_lshlrev_b32_sdwa v52, v200, sext(v55) dst_sel:DWORD dst_unused:UNUSED_PAD src0_sel:DWORD src1_sel:WORD_0
	v_ashrrev_i32_e32 v53, 31, v52
	v_lshl_add_u64 v[50:51], v[52:53], 1, v[50:51]
	global_load_dwordx4 v[108:111], v[50:51], off
	v_add_u32_e32 v56, 0x23f, v80
	s_movk_i32 s7, 0x47f
	v_mov_b32_e32 v57, s84
	v_mov_b32_e32 v58, s83
	v_cmp_gt_u32_e32 vcc, s7, v56
	v_mul_i32_i24_sdwa v54, sext(v54), s69 dst_sel:DWORD dst_unused:UNUSED_PAD src0_sel:WORD_0 src1_sel:DWORD
	v_lshlrev_b32_sdwa v55, v201, sext(v55) dst_sel:DWORD dst_unused:UNUSED_PAD src0_sel:DWORD src1_sel:WORD_0
	v_cndmask_b32_e32 v56, v57, v58, vcc
	v_add3_u32 v112, v56, v54, v55
.LBB0_616:
	s_or_b64 exec, exec, s[12:13]
	s_movk_i32 s7, 0x280
	v_cmp_gt_i32_e32 vcc, s7, v80
	s_and_saveexec_b64 s[12:13], vcc
	s_cbranch_execz .LBB0_618
	s_mov_b32 s7, 0x38e38e39
	v_mul_hi_i32 v50, v83, s7
	v_lshrrev_b32_e32 v51, 31, v50
	v_ashrrev_i32_e32 v50, 7, v50
	v_add_u32_e32 v50, v50, v51
	v_mul_i32_i24_e32 v51, 0x240, v50
	v_sub_u32_e32 v51, v83, v51
	v_mul_i32_i24_e32 v52, 0x2aab, v51
	v_lshrrev_b32_e32 v53, 31, v52
	v_add_u16_sdwa v54, v52, v53 dst_sel:DWORD dst_unused:UNUSED_PAD src0_sel:WORD_1 src1_sel:DWORD
	v_mul_lo_u16_e32 v52, 6, v54
	v_add_u32_e32 v50, s3, v50
	v_sub_u16_e32 v55, v51, v52
	v_lshl_or_b32 v52, v50, 6, s18
	v_mov_b64_e32 v[50:51], s[4:5]
	s_movk_i32 s7, 0x2400
	v_mad_i64_i32 v[50:51], s[14:15], v52, s7, v[50:51]
	v_mul_i32_i24_sdwa v52, sext(v54), v199 dst_sel:DWORD dst_unused:UNUSED_PAD src0_sel:WORD_0 src1_sel:DWORD
	v_ashrrev_i32_e32 v53, 31, v52
	v_lshl_add_u64 v[50:51], v[52:53], 1, v[50:51]
	v_lshlrev_b32_sdwa v52, v200, sext(v55) dst_sel:DWORD dst_unused:UNUSED_PAD src0_sel:DWORD src1_sel:WORD_0
	v_ashrrev_i32_e32 v53, 31, v52
	v_lshl_add_u64 v[50:51], v[52:53], 1, v[50:51]
	global_load_dwordx4 v[116:119], v[50:51], off
	v_add_u32_e32 v56, 0x43f, v80
	s_movk_i32 s7, 0x47f
	v_mov_b32_e32 v57, s84
	v_mov_b32_e32 v58, s83
	v_cmp_gt_u32_e32 vcc, s7, v56
	v_mul_i32_i24_sdwa v54, sext(v54), s69 dst_sel:DWORD dst_unused:UNUSED_PAD src0_sel:WORD_0 src1_sel:DWORD
	v_lshlrev_b32_sdwa v55, v201, sext(v55) dst_sel:DWORD dst_unused:UNUSED_PAD src0_sel:DWORD src1_sel:WORD_0
	v_cndmask_b32_e32 v56, v57, v58, vcc
	v_add3_u32 v113, v56, v54, v55

.LBB0_620:
	s_or_b64 exec, exec, s[12:13]
	s_waitcnt vmcnt(0)
	v_cmp_gt_i32_e32 vcc, 0x480, v80
	s_and_saveexec_b64 s[12:13], vcc
	ds_write_b128 v112, v[108:111]
	s_or_b64 exec, exec, s[12:13]
	v_cmp_gt_i32_e32 vcc, 0x280, v80
	s_and_saveexec_b64 s[12:13], vcc
	ds_write_b128 v113, v[116:119]
	s_or_b64 exec, exec, s[12:13]
	v_cndmask_b32_e64 v50, 0, 1, s[8:9]
	v_cmp_ne_u32_e64 s[4:5], 1, v50
	s_andn2_b64 vcc, exec, s[8:9]
	v_lshlrev_b32_e32 v178, 3, v175
	s_cbranch_vccnz .LBB0_622
	s_lshl_b32 s3, s19, 9
	s_lshl_b32 s7, s97, 7
	s_or_b32 s3, s3, s7
	v_lshl_add_u32 v52, v175, 1, s20
	v_mov_b64_e32 v[50:51], s[10:11]
	s_or_b32 s8, s3, s18
	s_mov_b32 s9, s41
	v_mad_i64_i32 v[50:51], s[10:11], v52, s67, v[50:51]
	s_mov_b32 s7, s41
	s_lshl_b64 s[8:9], s[8:9], 2
	v_lshl_add_u64 v[54:55], v[50:51], 0, s[6:7]
	s_add_u32 s80, s76, s8
	global_load_ushort v58, v[54:55], off offset:2312
	global_load_ushort v59, v[54:55], off offset:2328
	s_addc_u32 s81, s77, s9
	s_mov_b64 s[8:9], 0x1d00
	v_lshl_add_u64 v[52:53], v[50:51], 0, s[8:9]
	s_or_b32 s8, s6, 8
	s_mov_b32 s9, s41
	v_lshl_add_u64 v[50:51], v[52:53], 0, s[8:9]
	s_or_b32 s8, s6, 24
	v_lshl_add_u64 v[56:57], v[52:53], 0, s[8:9]
	global_load_ushort v60, v[50:51], off
	global_load_ushort v61, v[56:57], off
	v_and_b32_e32 v62, 64, v233
	v_add_u32_e32 v50, -1, v233
	v_add_u32_e32 v51, -2, v233
	v_cmp_lt_i32_e32 vcc, v50, v62
	v_add_u32_e32 v56, -4, v233
	s_or_b32 s8, s6, 16
	v_cndmask_b32_e32 v50, v50, v233, vcc
	v_cmp_lt_i32_e32 vcc, v51, v62
	v_lshlrev_b32_e32 v50, 2, v50
	v_cmp_gt_i32_e64 s[10:11], 2, v175
	v_cndmask_b32_e32 v51, v51, v233, vcc
	v_cmp_lt_i32_e32 vcc, v56, v62
	v_lshlrev_b32_e32 v63, 2, v51
	v_cmp_gt_i32_e64 s[16:17], 63, v175
	v_cndmask_b32_e32 v56, v56, v233, vcc
	v_lshlrev_b32_e32 v64, 2, v56
	v_lshl_add_u64 v[56:57], v[52:53], 0, s[6:7]
	v_lshl_add_u64 v[52:53], v[52:53], 0, s[8:9]
	global_load_ushort v56, v[56:57], off
	s_nop 0
	global_load_ushort v51, v[52:53], off
	s_nop 0
	global_load_ushort v52, v[54:55], off offset:2320
	global_load_ushort v53, v[54:55], off offset:2304
	v_cmp_gt_i32_e64 s[8:9], 1, v175
	v_cmp_gt_i32_e64 s[18:19], 62, v175
	v_cmp_gt_i32_e64 s[14:15], 16, v175
	v_cmp_gt_i32_e64 s[20:21], 60, v175
	v_cmp_gt_i32_e64 s[22:23], 56, v175
	global_load_dword v180, v254, s[80:81]
	global_load_dword v181, v254, s[80:81] offset:256
	v_cmp_gt_i32_e64 s[26:27], 48, v175
	s_waitcnt vmcnt(9)
	v_lshlrev_b32_e32 v54, 16, v58
	v_max_f32_e32 v57, v54, v54
	v_mul_f32_e64 v54, |v54|, s28
	s_waitcnt vmcnt(8)
	v_lshlrev_b32_e32 v55, 16, v59
	v_exp_f32_e32 v54, v54
	v_max_f32_e32 v58, v55, v55
	v_mul_f32_e64 v55, |v55|, s28
	v_exp_f32_e32 v55, v55
	v_add_f32_e32 v54, 1.0, v54
	s_waitcnt vmcnt(7)
	v_lshlrev_b32_e32 v59, 16, v60
	s_waitcnt vmcnt(6)
	v_lshlrev_b32_e32 v60, 16, v61
	v_max_f32_e32 v61, v59, v59
	v_mul_f32_e64 v59, |v59|, s28
	v_max_f32_e32 v65, v60, v60
	v_mul_f32_e64 v60, |v60|, s28
	v_exp_f32_e32 v59, v59
	v_exp_f32_e32 v60, v60
	v_cmp_gt_f32_e32 vcc, s55, v54
	v_add_f32_e32 v55, 1.0, v55
	v_cmp_gt_f32_e64 s[6:7], s55, v55
	v_cndmask_b32_e64 v70, 0, 32, vcc
	v_ldexp_f32 v54, v54, v70
	v_cndmask_b32_e64 v71, 0, 32, s[6:7]
	v_log_f32_e32 v54, v54
	v_add_f32_e32 v59, 1.0, v59
	v_ldexp_f32 v55, v55, v71
	v_cndmask_b32_e64 v71, 0, v232, s[6:7]
	v_add_f32_e32 v60, 1.0, v60
	v_cmp_gt_f32_e64 s[6:7], s55, v59
	v_cndmask_b32_e32 v70, 0, v232, vcc
	v_cmp_gt_f32_e32 vcc, s55, v60
	v_cndmask_b32_e64 v72, 0, 32, s[6:7]
	v_ldexp_f32 v59, v59, v72
	v_cndmask_b32_e64 v73, 0, 32, vcc
	v_ldexp_f32 v60, v60, v73
	v_mul_f32_e32 v73, 0x3f317217, v54
	v_log_f32_e32 v59, v59
	v_fma_f32 v73, v54, s94, -v73
	v_fmac_f32_e32 v73, 0x3377d1cf, v54
	v_cndmask_b32_e64 v72, 0, v232, s[6:7]
	v_fmac_f32_e32 v73, 0x3f317217, v54
	v_cmp_lt_f32_e64 s[6:7], |v54|, s95
	v_min_f32_e32 v57, 0, v57
	v_min_f32_e32 v61, 0, v61
	v_cndmask_b32_e64 v54, v54, v73, s[6:7]
	v_mul_f32_e32 v73, 0x3f317217, v59
	v_sub_f32_e32 v54, v54, v70
	v_fma_f32 v70, v59, s94, -v73
	v_fmac_f32_e32 v70, 0x3377d1cf, v59
	v_fmac_f32_e32 v70, 0x3f317217, v59
	v_cmp_lt_f32_e64 s[6:7], |v59|, s95
	v_sub_f32_e32 v57, v57, v54
	v_log_f32_e32 v55, v55
	v_cndmask_b32_e64 v54, v59, v70, s[6:7]
	v_sub_f32_e32 v54, v54, v72
	v_sub_f32_e32 v59, v61, v54
	v_add_f32_e32 v54, v57, v59
	ds_bpermute_b32 v61, v50, v54
	v_mul_f32_e32 v74, 0x3f317217, v55
	v_fma_f32 v70, v55, s94, -v74
	v_log_f32_e32 v60, v60
	v_fmac_f32_e32 v70, 0x3377d1cf, v55
	s_waitcnt lgkmcnt(0)
	v_add_f32_e32 v61, v54, v61
	v_cndmask_b32_e64 v54, v61, v54, s[8:9]
	ds_bpermute_b32 v61, v63, v54
	v_fmac_f32_e32 v70, 0x3f317217, v55
	v_cmp_lt_f32_e64 s[6:7], |v55|, s95
	v_min_f32_e32 v58, 0, v58
	v_min_f32_e32 v65, 0, v65
	s_waitcnt lgkmcnt(0)
	v_add_f32_e32 v61, v54, v61
	v_cndmask_b32_e64 v54, v61, v54, s[10:11]
	ds_bpermute_b32 v61, v64, v54
	v_cndmask_b32_e64 v55, v55, v70, s[6:7]
	v_sub_f32_e32 v55, v55, v71
	v_mul_f32_e32 v70, 0x3f317217, v60
	v_sub_f32_e32 v58, v58, v55
	s_waitcnt lgkmcnt(0)
	v_add_f32_e32 v55, v54, v61
	v_cmp_gt_i32_e64 s[6:7], 4, v175
	v_fma_f32 v70, v60, s94, -v70
	v_fmac_f32_e32 v70, 0x3377d1cf, v60
	v_cndmask_b32_e64 v54, v55, v54, s[6:7]
	v_add_u32_e32 v55, -8, v233
	v_cmp_lt_i32_e64 s[12:13], v55, v62
	v_fmac_f32_e32 v70, 0x3f317217, v60
	s_waitcnt vmcnt(3)
	v_lshlrev_b32_e32 v52, 16, v52
	v_cndmask_b32_e64 v55, v55, v233, s[12:13]
	v_cmp_lt_f32_e64 s[12:13], |v60|, s95
	v_lshlrev_b32_e32 v61, 2, v55
	ds_bpermute_b32 v55, v61, v54
	v_cndmask_b32_e64 v60, v60, v70, s[12:13]
	v_cndmask_b32_e32 v70, 0, v232, vcc
	v_sub_f32_e32 v60, v60, v70
	v_and_b32_e32 v70, 63, v233
	v_cmp_ne_u32_e64 s[12:13], 63, v70
	v_sub_f32_e32 v60, v65, v60
	v_add_f32_e32 v65, v58, v60
	v_addc_co_u32_e64 v71, s[12:13], 0, v233, s[12:13]
	v_lshlrev_b32_e32 v71, 2, v71
	ds_bpermute_b32 v72, v71, v65
	s_waitcnt lgkmcnt(1)
	v_add_f32_e32 v55, v54, v55
	v_cmp_gt_i32_e32 vcc, 8, v175
	v_cmp_gt_u32_e64 s[24:25], 48, v70
	s_waitcnt lgkmcnt(0)
	v_add_f32_e32 v72, v65, v72
	v_cndmask_b32_e32 v54, v55, v54, vcc
	v_add_u32_e32 v55, -16, v233
	v_cmp_lt_i32_e64 s[12:13], v55, v62
	v_cndmask_b32_e64 v65, v65, v72, s[16:17]
	s_nop 0
	v_cndmask_b32_e64 v55, v55, v233, s[12:13]
	v_cmp_gt_u32_e64 s[12:13], 62, v70
	v_lshlrev_b32_e32 v73, 2, v55
	ds_bpermute_b32 v55, v73, v54
	v_cndmask_b32_e64 v72, 0, 2, s[12:13]
	v_add_lshl_u32 v72, v72, v233, 2
	ds_bpermute_b32 v74, v72, v65
	v_cmp_gt_u32_e64 s[12:13], 60, v70
	s_waitcnt lgkmcnt(1)
	v_add_f32_e32 v55, v54, v55
	v_cndmask_b32_e64 v54, v55, v54, s[14:15]
	v_subrev_u32_e32 v55, 32, v233
	s_waitcnt lgkmcnt(0)
	v_add_f32_e32 v74, v65, v74
	v_cndmask_b32_e64 v65, v65, v74, s[18:19]
	v_cndmask_b32_e64 v74, 0, 4, s[12:13]
	v_add_lshl_u32 v74, v74, v233, 2
	ds_bpermute_b32 v75, v74, v65
	v_cmp_lt_i32_e64 s[12:13], v55, v62
	s_waitcnt lgkmcnt(0)
	v_add_f32_e32 v75, v65, v75
	v_cndmask_b32_e64 v55, v55, v233, s[12:13]
	v_cmp_gt_u32_e64 s[12:13], 56, v70
	v_lshlrev_b32_e32 v62, 2, v55
	v_cndmask_b32_e64 v65, v65, v75, s[20:21]
	v_cndmask_b32_e64 v75, 0, 8, s[12:13]
	ds_bpermute_b32 v55, v62, v54
	v_add_lshl_u32 v75, v75, v233, 2
	ds_bpermute_b32 v76, v75, v65
	v_cmp_gt_i32_e64 s[12:13], 32, v175
	s_waitcnt lgkmcnt(1)
	v_add_f32_e32 v55, v54, v55
	v_cndmask_b32_e64 v54, v55, v54, s[12:13]
	s_waitcnt lgkmcnt(0)
	v_add_f32_e32 v55, v65, v76
	v_cndmask_b32_e64 v65, v65, v55, s[22:23]
	v_cndmask_b32_e64 v55, 0, 16, s[24:25]
	ds_bpermute_b32 v54, v50, v54
	v_add_lshl_u32 v70, v55, v233, 2
	ds_bpermute_b32 v55, v70, v65
	v_cmp_eq_u32_e64 s[24:25], 0, v175
	s_waitcnt lgkmcnt(0)
	v_add_f32_e32 v77, v65, v55
	v_cndmask_b32_e64 v76, v54, 0, s[24:25]
	v_lshlrev_b32_e32 v55, 16, v56
	v_add_f32_e32 v56, v57, v76
	s_waitcnt vmcnt(2)
	v_lshlrev_b32_e32 v54, 16, v53
	v_add_f32_e32 v57, v59, v56
	v_pk_add_f32 v[54:55], v[54:55], v[56:57] neg_lo:[0,1] neg_hi:[0,1]
	v_mov_b32_e32 v76, 0x80
	v_max_f32_e32 v53, v54, v55
	ds_bpermute_b32 v59, v50, v53
	v_cndmask_b32_e64 v65, v65, v77, s[26:27]
	v_lshl_or_b32 v76, v233, 2, v76
	ds_bpermute_b32 v77, v76, v65
	s_waitcnt lgkmcnt(1)
	v_max_f32_e32 v59, v59, v59
	v_max_f32_e32 v59, v53, v59
	v_cndmask_b32_e64 v53, v59, v53, s[8:9]
	ds_bpermute_b32 v59, v63, v53
	s_waitcnt lgkmcnt(1)
	v_add_f32_e32 v63, v65, v77
	v_cndmask_b32_e64 v63, v65, v63, s[12:13]
	ds_bpermute_b32 v63, v71, v63
	v_cmp_eq_u32_e64 s[8:9], 63, v175
	s_waitcnt lgkmcnt(1)
	v_max_f32_e32 v59, v59, v59
	v_max_f32_e32 v59, v53, v59
	v_cndmask_b32_e64 v53, v59, v53, s[10:11]
	ds_bpermute_b32 v59, v64, v53
	s_waitcnt lgkmcnt(1)
	v_cndmask_b32_e64 v63, v63, 0, s[8:9]
	s_waitcnt lgkmcnt(0)
	v_max_f32_e32 v59, v59, v59
	v_max_f32_e32 v59, v53, v59
	v_cndmask_b32_e64 v64, v59, v53, s[6:7]
	v_add_f32_e32 v59, v60, v63
	v_lshlrev_b32_e32 v53, 16, v51
	v_add_f32_e32 v58, v58, v59
	v_pk_add_f32 v[52:53], v[52:53], v[58:59] neg_lo:[0,1] neg_hi:[0,1]
	ds_bpermute_b32 v61, v61, v64
	v_max_f32_e32 v51, v52, v53
	ds_bpermute_b32 v60, v71, v51
	s_mov_b32 s6, 0x3fb8aa3b
	s_waitcnt lgkmcnt(1)
	v_max_f32_e32 v61, v61, v61
	v_max_f32_e32 v61, v64, v61
	s_waitcnt lgkmcnt(0)
	v_max_f32_e32 v60, v60, v60
	v_max_f32_e32 v60, v51, v60
	v_cndmask_b32_e64 v51, v51, v60, s[16:17]
	ds_bpermute_b32 v60, v72, v51
	v_cndmask_b32_e32 v61, v61, v64, vcc
	ds_bpermute_b32 v63, v73, v61
	s_waitcnt lgkmcnt(1)
	v_max_f32_e32 v60, v60, v60
	v_max_f32_e32 v60, v51, v60
	v_cndmask_b32_e64 v51, v51, v60, s[18:19]
	ds_bpermute_b32 v60, v74, v51
	s_waitcnt lgkmcnt(1)
	v_max_f32_e32 v63, v63, v63
	v_max_f32_e32 v63, v61, v63
	v_cndmask_b32_e64 v61, v63, v61, s[14:15]
	ds_bpermute_b32 v62, v62, v61
	s_waitcnt lgkmcnt(1)
	v_max_f32_e32 v60, v60, v60
	v_max_f32_e32 v60, v51, v60
	v_cndmask_b32_e64 v51, v51, v60, s[20:21]
	ds_bpermute_b32 v60, v75, v51
	v_max_f32_e32 v63, v61, v61
	s_waitcnt lgkmcnt(1)
	v_max_f32_e32 v62, v62, v62
	v_max_f32_e32 v62, v63, v62
	v_cndmask_b32_e64 v61, v62, v61, s[12:13]
	s_waitcnt lgkmcnt(0)
	v_max_f32_e32 v60, v60, v60
	v_max_f32_e32 v60, v51, v60
	v_cndmask_b32_e64 v51, v51, v60, s[22:23]
	ds_bpermute_b32 v60, v70, v51
	ds_bpermute_b32 v50, v50, v61
	v_add_u32_e32 v61, s85, v178
	v_add_u32_e32 v62, s45, v178
	ds_write_b64 v61, v[56:57]
	s_waitcnt lgkmcnt(2)
	v_max_f32_e32 v60, v60, v60
	v_max_f32_e32 v60, v51, v60
	v_cndmask_b32_e64 v51, v51, v60, s[26:27]
	ds_bpermute_b32 v60, v76, v51
	s_waitcnt lgkmcnt(2)
	v_cndmask_b32_e64 v50, v50, v241, s[24:25]
	v_max_f32_e32 v50, v50, v50
	v_max_f32_e32 v63, v50, v54
	v_max_f32_e32 v50, v51, v51
	s_waitcnt lgkmcnt(0)
	v_max_f32_e32 v60, v60, v60
	v_max_f32_e32 v50, v50, v60
	v_cndmask_b32_e64 v50, v51, v50, s[12:13]
	ds_bpermute_b32 v60, v71, v50
	v_pk_mul_f32 v[50:51], v[54:55], s[6:7] op_sel_hi:[1,0]
	v_add_u32_e32 v54, s38, v178
	ds_write_b64 v54, v[50:51]
	v_max_f32_e32 v64, v63, v55
	s_waitcnt lgkmcnt(1)
	v_cndmask_b32_e64 v50, v60, v241, s[8:9]
	v_max_f32_e32 v50, v50, v50
	v_max_f32_e32 v54, v50, v53
	v_max_f32_e32 v55, v54, v52
	v_pk_mul_f32 v[50:51], v[52:53], s[6:7] op_sel_hi:[1,0]
	v_add_u32_e32 v52, s39, v178
	ds_write_b64 v52, v[50:51]
	s_waitcnt vmcnt(1)
	v_add_f32_e32 v50, v180, v56
	v_add_f32_e32 v51, v56, v63
	v_max_f32_e32 v50, v50, v51
	v_add_f32_e32 v51, v180, v57
	v_add_f32_e32 v52, v57, v64
	v_max_f32_e32 v51, v51, v52
	v_add_u32_e32 v52, s89, v178
	ds_write_b64 v52, v[50:51]
	s_waitcnt vmcnt(0)
	v_add_f32_e32 v50, v181, v58
	v_add_f32_e32 v51, v58, v55
	v_max_f32_e32 v50, v50, v51
	v_add_f32_e32 v51, v181, v59
	v_add_f32_e32 v52, v59, v54
	v_max_f32_e32 v51, v51, v52
	v_add_u32_e32 v52, s54, v178
	ds_write_b64 v62, v[58:59]
	ds_write_b64 v52, v[50:51]
	s_branch .LBB0_623

.Li_tiles_done:
	s_load_dwordx2 s[12:13], s[0:1], 0x48
	s_load_dwordx2 s[10:11], s[0:1], 0x50
	s_load_dwordx2 s[14:15], s[0:1], 0x88
	s_load_dwordx2 s[18:19], s[0:1], 0x90
	s_load_dwordx2 s[8:9], s[0:1], 0x98
	s_lshl_b32 s39, s3, 3
	s_add_i32 s4, s29, s39
	s_cmpk_gt_i32 s4, 0x7fff
	s_cbranch_scc1 .LBB0_1281
	s_add_u32 s45, s6, 0x5d200000
	s_addc_u32 s54, s7, 0
	s_lshl_b32 s40, s74, 10
	s_lshl_b64 s[16:17], s[40:41], 2
	v_lshlrev_b32_e32 v30, 2, v2
	s_waitcnt lgkmcnt(0)
	s_add_u32 s12, s12, s16
	v_ashrrev_i32_e32 v31, 31, v30
	s_addc_u32 s13, s13, s17
	v_lshlrev_b64 v[14:15], 2, v[30:31]
	v_lshl_add_u64 v[6:7], s[12:13], 0, v[14:15]
	global_load_dwordx4 v[100:103], v[6:7], off
	s_add_u32 s10, s10, s16
	s_addc_u32 s11, s11, s17
	v_lshl_add_u64 v[8:9], s[10:11], 0, v[14:15]
	global_load_dwordx4 v[104:107], v[8:9], off
	global_load_dwordx4 v[108:111], v[6:7], off offset:1024
	global_load_dwordx4 v[112:115], v[8:9], off offset:1024
	global_load_dwordx4 v[116:119], v[6:7], off offset:2048
	global_load_dwordx4 v[120:123], v[8:9], off offset:2048
	global_load_dwordx4 v[124:127], v[6:7], off offset:3072
	global_load_dwordx4 v[2:5], v[8:9], off offset:3072
	s_add_u32 s10, s6, 0x83200000
	s_addc_u32 s11, s7, 0
	s_add_u32 s40, s6, 0x94200000
	s_addc_u32 s56, s7, 0
	s_add_u32 s57, s6, 0x94300000
	s_addc_u32 s75, s7, 0
	s_add_u32 s80, s6, 0x94400000
	s_addc_u32 s81, s7, 0
	s_lshl_b32 s5, s24, 3
	s_add_u32 s82, s6, 0x3a200000
	s_addc_u32 s83, s7, 0
	s_lshl_b32 s59, s24, 4
	s_add_u32 s12, s6, 0x4d200000
	s_addc_u32 s13, s7, 0
	s_add_i32 s5, s4, s5
	s_min_i32 s20, s5, 0x7fff
	s_ashr_i32 s21, s20, 31
	s_lshl_b64 s[22:23], s[20:21], 11
	s_add_u32 s22, s12, s22
	s_addc_u32 s23, s13, s23
	v_lshlrev_b64 v[16:17], 1, v[30:31]
	v_lshl_add_u64 v[78:79], s[12:13], 0, v[16:17]
	s_mul_i32 s89, s24, 40
	s_waitcnt vmcnt(0)
	v_pk_mul_f32 v[32:33], v[102:103], s[66:67] op_sel_hi:[1,0]
	v_pk_mul_f32 v[34:35], v[100:101], s[66:67] op_sel_hi:[1,0]
	v_pk_mul_f32 v[36:37], v[106:107], s[66:67] op_sel_hi:[1,0]
	v_pk_mul_f32 v[38:39], v[104:105], s[66:67] op_sel_hi:[1,0]
	v_pk_mul_f32 v[40:41], v[110:111], s[66:67] op_sel_hi:[1,0]
	v_pk_mul_f32 v[42:43], v[108:109], s[66:67] op_sel_hi:[1,0]
	v_pk_mul_f32 v[44:45], v[114:115], s[66:67] op_sel_hi:[1,0]
	v_pk_mul_f32 v[46:47], v[112:113], s[66:67] op_sel_hi:[1,0]
	v_pk_mul_f32 v[48:49], v[118:119], s[66:67] op_sel_hi:[1,0]
	v_pk_mul_f32 v[50:51], v[116:117], s[66:67] op_sel_hi:[1,0]
	v_pk_mul_f32 v[52:53], v[122:123], s[66:67] op_sel_hi:[1,0]
	v_pk_mul_f32 v[54:55], v[120:121], s[66:67] op_sel_hi:[1,0]
	v_pk_mul_f32 v[56:57], v[126:127], s[66:67] op_sel_hi:[1,0]
	v_pk_mul_f32 v[58:59], v[124:125], s[66:67] op_sel_hi:[1,0]
	v_pk_mul_f32 v[62:63], v[2:3], s[66:67] op_sel_hi:[1,0]
	v_lshl_add_u64 v[2:3], s[22:23], 0, v[16:17]
	s_lshl_b64 s[22:23], s[20:21], 3
	s_add_u32 s22, s45, s22
	s_addc_u32 s23, s54, s23
	s_lshl_b32 s20, s20, 2
	s_ashr_i32 s21, s20, 31
	s_lshl_b64 s[20:21], s[20:21], 2
	global_load_dwordx2 v[64:65], v[2:3], off offset:1536
	global_load_dwordx2 v[72:73], v[2:3], off offset:1024
	global_load_dwordx2 v[74:75], v[2:3], off offset:512
	global_load_dwordx2 v[76:77], v[2:3], off
	global_load_dwordx2 v[70:71], v215, s[22:23]
	s_add_u32 s22, s40, s20
	s_addc_u32 s23, s56, s21
	v_pk_mul_f32 v[60:61], v[4:5], s[66:67] op_sel_hi:[1,0]
	global_load_dwordx4 v[2:5], v215, s[22:23]
	s_add_u32 s22, s80, s20
	s_addc_u32 s23, s81, s21
	s_add_u32 s20, s57, s20
	s_addc_u32 s21, s75, s21
	s_add_u32 s18, s18, s16
	s_addc_u32 s19, s19, s17
	s_ashr_i32 s5, s4, 31
	v_lshl_add_u64 v[82:83], s[18:19], 0, v[14:15]
	s_waitcnt vmcnt(0)
	v_lshlrev_b32_e32 v5, 2, v5
	v_add_u32_e32 v5, s38, v5
	ds_read_b32 v6, v5
	v_lshlrev_b32_e32 v4, 2, v4
	v_add_u32_e32 v4, s38, v4
	v_lshlrev_b32_e32 v3, 2, v3
	v_add_u32_e32 v3, s38, v3
	s_waitcnt lgkmcnt(0)
	v_ashrrev_i32_e32 v7, 31, v6
	v_lshlrev_b64 v[6:7], 18, v[6:7]
	v_lshl_add_u64 v[10:11], s[10:11], 0, v[6:7]
	global_load_dwordx4 v[6:9], v215, s[22:23]
	v_lshlrev_b32_e32 v2, 2, v2
	v_add_u32_e32 v2, s38, v2
	s_lshl_b64 s[22:23], s[4:5], 11
	s_waitcnt vmcnt(0)
	v_mov_b32_e32 v214, v9
	v_lshlrev_b64 v[12:13], 10, v[214:215]
	v_lshl_add_u64 v[10:11], v[10:11], 0, v[12:13]
	v_lshl_add_u64 v[10:11], v[10:11], 0, v[30:31]
	global_load_dword v122, v[10:11], off offset:768
	global_load_dword v123, v[10:11], off offset:512
	global_load_dword v124, v[10:11], off offset:256
	global_load_dword v125, v[10:11], off
	ds_read_b32 v4, v4
	v_mov_b32_e32 v9, v215
	v_lshlrev_b64 v[8:9], 10, v[8:9]
	v_mov_b32_e32 v214, v7
	v_mov_b32_e32 v7, v215
	s_waitcnt lgkmcnt(0)
	v_ashrrev_i32_e32 v5, 31, v4
	v_lshlrev_b64 v[4:5], 18, v[4:5]
	v_lshl_add_u64 v[4:5], s[10:11], 0, v[4:5]
	v_lshl_add_u64 v[4:5], v[4:5], 0, v[8:9]
	v_lshl_add_u64 v[4:5], v[4:5], 0, v[30:31]
	global_load_dword v118, v[4:5], off offset:768
	global_load_dword v119, v[4:5], off offset:512
	global_load_dword v120, v[4:5], off offset:256
	global_load_dword v121, v[4:5], off
	ds_read_b32 v4, v3
	v_lshlrev_b64 v[8:9], 10, v[214:215]
	s_waitcnt lgkmcnt(0)
	v_ashrrev_i32_e32 v5, 31, v4
	v_lshlrev_b64 v[4:5], 18, v[4:5]
	v_lshl_add_u64 v[4:5], s[10:11], 0, v[4:5]
	v_lshl_add_u64 v[4:5], v[4:5], 0, v[8:9]
	v_lshl_add_u64 v[4:5], v[4:5], 0, v[30:31]
	global_load_dword v114, v[4:5], off offset:768
	global_load_dword v115, v[4:5], off offset:512
	global_load_dword v116, v[4:5], off offset:256
	global_load_dword v117, v[4:5], off
	ds_read_b32 v2, v2
	v_lshlrev_b64 v[4:5], 10, v[6:7]
	s_waitcnt lgkmcnt(0)
	v_ashrrev_i32_e32 v3, 31, v2
	v_lshlrev_b64 v[2:3], 18, v[2:3]
	v_lshl_add_u64 v[2:3], s[10:11], 0, v[2:3]
	v_lshl_add_u64 v[2:3], v[2:3], 0, v[4:5]
	v_lshl_add_u64 v[2:3], v[2:3], 0, v[30:31]
	global_load_dword v110, v[2:3], off offset:768
	global_load_dword v111, v[2:3], off offset:512
	global_load_dword v112, v[2:3], off offset:256
	global_load_dword v113, v[2:3], off
	global_load_dwordx4 v[10:13], v215, s[20:21]
	s_add_u32 s20, s12, s22
	s_addc_u32 s21, s13, s23
	v_lshl_add_u64 v[2:3], s[20:21], 0, v[16:17]
	s_lshl_b64 s[20:21], s[4:5], 3
	s_add_u32 s20, s45, s20
	s_addc_u32 s21, s54, s21
	global_load_dwordx2 v[84:85], v[2:3], off offset:1536
	global_load_dwordx2 v[88:89], v[2:3], off offset:1024
	global_load_dwordx2 v[90:91], v[2:3], off offset:512
	global_load_dwordx2 v[92:93], v[2:3], off
	global_load_dwordx2 v[86:87], v215, s[20:21]
	s_add_u32 s20, s14, s16
	s_addc_u32 s21, s15, s17
	s_lshl_b32 s14, s4, 2
	s_ashr_i32 s15, s14, 31
	s_lshl_b64 s[14:15], s[14:15], 2
	s_add_u32 s16, s40, s14
	s_addc_u32 s17, s56, s15
	global_load_dwordx4 v[2:5], v215, s[16:17]
	s_add_u32 s16, s80, s14
	s_addc_u32 s17, s81, s15
	s_add_u32 s14, s57, s14
	s_addc_u32 s15, s75, s15
	v_and_b32_e32 v16, 64, v233
	v_add_u32_e32 v16, 64, v16
	v_xor_b32_e32 v17, 1, v233
	v_cmp_lt_i32_e32 vcc, v17, v16
	s_mul_i32 s12, s24, 24
	v_lshl_add_u64 v[80:81], s[20:21], 0, v[14:15]
	v_cndmask_b32_e32 v17, v233, v17, vcc
	v_lshlrev_b32_e32 v126, 2, v17
	v_xor_b32_e32 v17, 2, v233
	v_cmp_lt_i32_e32 vcc, v17, v16
	s_waitcnt vmcnt(0)
	v_lshlrev_b32_e32 v5, 2, v5
	v_add_u32_e32 v5, s38, v5
	ds_read_b32 v6, v5
	v_lshlrev_b32_e32 v4, 2, v4
	v_add_u32_e32 v4, s38, v4
	v_lshlrev_b32_e32 v3, 2, v3
	v_add_u32_e32 v3, s38, v3
	s_waitcnt lgkmcnt(0)
	v_ashrrev_i32_e32 v7, 31, v6
	v_lshlrev_b64 v[6:7], 18, v[6:7]
	v_lshl_add_u64 v[18:19], s[10:11], 0, v[6:7]
	global_load_dwordx4 v[6:9], v215, s[16:17]
	v_lshlrev_b32_e32 v2, 2, v2
	v_add_u32_e32 v2, s38, v2
	v_cndmask_b32_e32 v17, v233, v17, vcc
	v_lshlrev_b32_e32 v127, 2, v17
	v_xor_b32_e32 v17, 4, v233
	v_cmp_lt_i32_e32 vcc, v17, v16
	s_waitcnt vmcnt(0)
	v_mov_b32_e32 v214, v9
	v_lshlrev_b64 v[20:21], 10, v[214:215]
	v_lshl_add_u64 v[18:19], v[18:19], 0, v[20:21]
	v_lshl_add_u64 v[18:19], v[18:19], 0, v[30:31]
	global_load_dword v132, v[18:19], off offset:768
	global_load_dword v133, v[18:19], off offset:512
	global_load_dword v134, v[18:19], off offset:256
	global_load_dword v135, v[18:19], off
	ds_read_b32 v4, v4
	v_mov_b32_e32 v9, v215
	v_lshlrev_b64 v[8:9], 10, v[8:9]
	v_mov_b32_e32 v214, v7
	v_mov_b32_e32 v7, v215
	s_waitcnt lgkmcnt(0)
	v_ashrrev_i32_e32 v5, 31, v4
	v_lshlrev_b64 v[4:5], 18, v[4:5]
	v_lshl_add_u64 v[4:5], s[10:11], 0, v[4:5]
	v_lshl_add_u64 v[4:5], v[4:5], 0, v[8:9]
	v_lshl_add_u64 v[4:5], v[4:5], 0, v[30:31]
	global_load_dword v144, v[4:5], off offset:768
	global_load_dword v145, v[4:5], off offset:512
	global_load_dword v146, v[4:5], off offset:256
	global_load_dword v147, v[4:5], off
	ds_read_b32 v4, v3
	v_lshlrev_b64 v[8:9], 10, v[214:215]
	v_cndmask_b32_e32 v17, v233, v17, vcc
	v_lshlrev_b32_e32 v128, 2, v17
	v_xor_b32_e32 v17, 8, v233
	s_waitcnt lgkmcnt(0)
	v_ashrrev_i32_e32 v5, 31, v4
	v_lshlrev_b64 v[4:5], 18, v[4:5]
	v_lshl_add_u64 v[4:5], s[10:11], 0, v[4:5]
	v_lshl_add_u64 v[4:5], v[4:5], 0, v[8:9]
	v_lshl_add_u64 v[4:5], v[4:5], 0, v[30:31]
	global_load_dword v140, v[4:5], off offset:768
	global_load_dword v141, v[4:5], off offset:512
	global_load_dword v142, v[4:5], off offset:256
	global_load_dword v143, v[4:5], off
	ds_read_b32 v2, v2
	v_lshlrev_b64 v[4:5], 10, v[6:7]
	v_cmp_lt_i32_e32 vcc, v17, v16
	s_waitcnt lgkmcnt(0)
	v_ashrrev_i32_e32 v3, 31, v2
	v_lshlrev_b64 v[2:3], 18, v[2:3]
	v_lshl_add_u64 v[2:3], s[10:11], 0, v[2:3]
	v_lshl_add_u64 v[2:3], v[2:3], 0, v[4:5]
	v_lshl_add_u64 v[2:3], v[2:3], 0, v[30:31]
	global_load_dword v136, v[2:3], off offset:768
	global_load_dword v137, v[2:3], off offset:512
	global_load_dword v138, v[2:3], off offset:256
	global_load_dword v139, v[2:3], off
	v_cndmask_b32_e32 v17, v233, v17, vcc
	global_load_dwordx4 v[2:5], v215, s[14:15]
	s_add_i32 s14, s4, s59
	s_min_i32 s14, s14, 0x7fff
	s_lshl_b32 s14, s14, 2
	s_ashr_i32 s15, s14, 31
	s_lshl_b64 s[14:15], s[14:15], 2
	s_add_u32 s16, s57, s14
	s_addc_u32 s17, s75, s15
	global_load_dwordx4 v[6:9], v215, s[16:17]
	s_add_u32 s16, s80, s14
	s_addc_u32 s17, s81, s15
	s_add_u32 s14, s40, s14
	s_addc_u32 s15, s56, s15
	global_load_dwordx4 v[18:21], v215, s[16:17]
	global_load_dwordx4 v[22:25], v215, s[14:15]
	s_cmp_eq_u32 s74, 3
	s_cselect_b64 s[14:15], -1, 0
	s_cmp_lg_u32 s74, 3
	s_cselect_b64 s[16:17], -1, 0
	s_add_u32 s84, s6, 0x32200000
	s_addc_u32 s85, s7, 0
	s_lshl_b32 s60, s24, 5
	s_add_i32 s24, s24, s3
	s_add_i32 s89, s89, s39
	s_lshl_b32 s97, s24, 3
	s_add_i32 s60, s60, s39
	s_lshl_b64 s[6:7], s[4:5], 10
	v_lshlrev_b32_e32 v129, 2, v17
	v_xor_b32_e32 v17, 16, v233
	s_add_u32 s61, s84, s6
	v_cmp_lt_i32_e32 vcc, v17, v16
	s_addc_u32 s65, s85, s7
	s_ashr_i32 s13, s12, 31
	v_cndmask_b32_e32 v17, v233, v17, vcc
	s_lshl_b64 s[18:19], s[12:13], 10
	s_lshl_b64 s[4:5], s[4:5], 12
	v_lshlrev_b32_e32 v130, 2, v17
	v_xor_b32_e32 v17, 32, v233
	s_add_u32 s62, s8, s4
	v_cmp_lt_i32_e32 vcc, v17, v16
	s_addc_u32 s63, s9, s5
	s_lshl_b64 s[20:21], s[12:13], 12
	v_cndmask_b32_e32 v16, v233, v17, vcc
	s_add_u32 s33, s82, s22
	v_lshlrev_b32_e32 v131, 2, v16
	s_addc_u32 s3, s83, s23
	s_lshl_b64 s[22:23], s[12:13], 11
	s_add_i32 s13, s12, s39
	s_add_i32 s59, s59, s39
	global_load_dwordx4 v[174:177], v[80:81], off
	global_load_dwordx4 v[192:195], v[82:83], off
	global_load_dwordx4 v[178:181], v[80:81], off offset:1024
	global_load_dwordx4 v[196:199], v[82:83], off offset:1024
	global_load_dwordx4 v[182:185], v[80:81], off offset:2048
	global_load_dwordx4 v[202:205], v[82:83], off offset:2048
	global_load_dwordx4 v[186:189], v[80:81], off offset:3072
	global_load_dwordx4 v[206:209], v[82:83], off offset:3072
	s_branch .LBB0_1230
